# baseline (speedup 1.0000x reference)
.Lk2_nodred:
	s_or_b64 exec, exec, s[2:3]
	v_lshrrev_b32_e32 v6, 3, v0
	v_and_b32_e32 v7, 7, v0
	v_lshrrev_b32_e32 v8, 8, v0
	v_bfe_u32 v9, v0, 3, 5
	v_lshlrev_b32_e32 v10, 2, v9
	v_lshl_or_b32 v10, v8, 7, v10
	v_add_u32_e32 v10, 0x10800, v10
	v_mul_u32_u24_e32 v11, 0x1080, v8
	v_mul_u32_u24_e32 v12, 0x210, v7
	v_lshlrev_b32_e32 v13, 4, v9
	v_add3_u32 v11, v11, v12, v13
	s_lshl_b32 s4, s18, 6
	v_or_b32_e32 v14, s4, v6
	v_mov_b32_e32 v15, 0
	v_lshlrev_b64 v[16:17], 8, v[14:15]
	v_lshl_add_u64 v[16:17], s[12:13], 0, v[16:17]
	s_lshl_b32 s2, s16, 7
	s_mov_b32 s3, 0
	v_lshl_add_u64 v[16:17], v[16:17], 0, s[2:3]
	v_lshlrev_b32_e32 v14, 4, v7
	v_lshl_add_u64 v[16:17], v[16:17], 0, v[14:15]
	s_waitcnt lgkmcnt(0)
	s_barrier
	ds_read_b32 v50, v10
	ds_read_b32 v51, v10 offset:256
	ds_read_b32 v52, v10 offset:512
	ds_read_b32 v53, v10 offset:768
	ds_read_b32 v54, v10 offset:1024
	ds_read_b32 v55, v10 offset:1280
	ds_read_b32 v56, v10 offset:1536
	ds_read_b32 v57, v10 offset:1792
	ds_read_b128 v[18:21], v11
	ds_read_b128 v[22:25], v11 offset:8448
	ds_read_b128 v[26:29], v11 offset:16896
	ds_read_b128 v[30:33], v11 offset:25344
	ds_read_b128 v[34:37], v11 offset:33792
	ds_read_b128 v[38:41], v11 offset:42240
	ds_read_b128 v[42:45], v11 offset:50688
	s_waitcnt lgkmcnt(13)
	ds_read_b128 v[46:49], v11 offset:59136
	v_add_f32_e32 v2, v50, v51
	s_waitcnt lgkmcnt(13)
	v_add_f32_e32 v2, v2, v52
	s_waitcnt lgkmcnt(12)
	v_add_f32_e32 v2, v2, v53
	s_waitcnt lgkmcnt(11)
	v_add_f32_e32 v2, v2, v54
	s_waitcnt lgkmcnt(10)
	v_add_f32_e32 v2, v2, v55
	s_waitcnt lgkmcnt(9)
	v_add_f32_e32 v2, v2, v56
	s_waitcnt lgkmcnt(8)
	v_add_f32_e32 v2, v2, v57
	v_div_scale_f32 v3, s[2:3], v2, v2, 1.0
	v_rcp_f32_e32 v4, v3
	v_div_scale_f32 v5, vcc, 1.0, v2, 1.0
	v_fma_f32 v6, -v3, v4, 1.0
	v_fmac_f32_e32 v4, v6, v4
	v_mul_f32_e32 v6, v5, v4
	v_fma_f32 v7, -v3, v6, v5
	v_fmac_f32_e32 v6, v7, v4
	v_fma_f32 v3, -v3, v6, v5
	v_div_fmas_f32 v3, v3, v4, v6
	v_div_fixup_f32 v8, v3, v2, 1.0
	s_waitcnt lgkmcnt(6)
	v_pk_add_f32 v[60:61], v[20:21], v[24:25]
	v_pk_add_f32 v[58:59], v[18:19], v[22:23]
	s_waitcnt lgkmcnt(5)
	v_pk_add_f32 v[60:61], v[60:61], v[28:29]
	v_pk_add_f32 v[58:59], v[58:59], v[26:27]
	s_waitcnt lgkmcnt(4)
	v_pk_add_f32 v[60:61], v[60:61], v[32:33]
	v_pk_add_f32 v[58:59], v[58:59], v[30:31]
	s_waitcnt lgkmcnt(3)
	v_pk_add_f32 v[60:61], v[60:61], v[36:37]
	v_pk_add_f32 v[58:59], v[58:59], v[34:35]
	s_waitcnt lgkmcnt(2)
	v_pk_add_f32 v[60:61], v[60:61], v[40:41]
	v_pk_add_f32 v[58:59], v[58:59], v[38:39]
	s_waitcnt lgkmcnt(1)
	v_pk_add_f32 v[60:61], v[60:61], v[44:45]
	v_pk_add_f32 v[58:59], v[58:59], v[42:43]
	s_waitcnt lgkmcnt(0)
	v_pk_add_f32 v[60:61], v[60:61], v[48:49]
	v_pk_add_f32 v[58:59], v[58:59], v[46:47]
	v_pk_mul_f32 v[60:61], v[60:61], v[8:9] op_sel_hi:[1,0]
	v_pk_mul_f32 v[58:59], v[58:59], v[8:9] op_sel_hi:[1,0]
	global_store_dwordx4 v[16:17], v[58:61], off
	s_endpgm
